# topk: the four key reads of a pass issued together with counted lgkmcnt waits (on top of v27)
# baseline (speedup 1.0000x reference)
.LBB0_924:
	v_add_u32_e32 v7, s5, v14
	ds_read2_b32 v[16:17], v7 offset1:16
	ds_read2_b32 v[124:125], v7 offset0:32 offset1:48
	ds_read2_b32 v[126:127], v7 offset0:64 offset1:80
	ds_read2_b32 v[128:129], v7 offset0:96 offset1:112
	s_movk_i32 s14, 0x7f
	s_waitcnt lgkmcnt(3)
	v_cmp_lt_i32_e32 vcc, -1, v16
	s_nop 1
	v_cndmask_b32_e32 v15, -1, v213, vcc
	v_cmp_lt_i32_e32 vcc, -1, v17
	v_bitop3_b32 v15, v15, s35, v16 bitop3:0x48
	v_bitop3_b32 v15, v15, s14, v77 bitop3:0x36
	v_cndmask_b32_e32 v16, -1, v213, vcc
	v_bitop3_b32 v16, v16, s35, v17 bitop3:0x48
	v_sub_u32_e32 v16, v16, v77
	v_add_u32_e32 v18, 0x6f, v16
	s_waitcnt lgkmcnt(2)
	v_mov_b32_e32 v16, v124
	v_mov_b32_e32 v17, v125
	s_mov_b64 s[14:15], -1
	s_nop 0
	v_cmp_lt_i32_e32 vcc, -1, v16
	s_nop 1
	v_cndmask_b32_e32 v19, -1, v213, vcc
	v_bitop3_b32 v16, v19, s35, v16 bitop3:0x48
	v_sub_u32_e32 v16, v16, v77
	v_cmp_lt_i32_e32 vcc, -1, v17
	v_add_u32_e32 v19, 0x5f, v16
	s_nop 0
	v_cndmask_b32_e32 v16, -1, v213, vcc
	v_bitop3_b32 v16, v16, s35, v17 bitop3:0x48
	v_sub_u32_e32 v16, v16, v77
	v_add_u32_e32 v20, 0x4f, v16
	s_waitcnt lgkmcnt(1)
	v_mov_b32_e32 v16, v126
	v_mov_b32_e32 v17, v127
	s_nop 0
	v_cmp_lt_i32_e32 vcc, -1, v16
	s_nop 1
	v_cndmask_b32_e32 v21, -1, v213, vcc
	v_bitop3_b32 v16, v21, s35, v16 bitop3:0x48
	v_cmp_lt_i32_e32 vcc, -1, v17
	v_bitop3_b32 v21, v16, 63, v77 bitop3:0x36
	s_nop 0
	v_cndmask_b32_e32 v16, -1, v213, vcc
	v_bitop3_b32 v16, v16, s35, v17 bitop3:0x48
	v_sub_u32_e32 v16, v16, v77
	v_add_u32_e32 v22, 47, v16
	s_waitcnt lgkmcnt(0)
	v_mov_b32_e32 v16, v128
	v_mov_b32_e32 v17, v129
	s_nop 0
	v_cmp_lt_i32_e32 vcc, -1, v16
	s_nop 1
	v_cndmask_b32_e32 v7, -1, v213, vcc
	v_cmp_lt_i32_e32 vcc, -1, v17
	v_bitop3_b32 v7, v7, s35, v16 bitop3:0x48
	v_bitop3_b32 v7, v7, 31, v77 bitop3:0x36
	v_cndmask_b32_e32 v16, -1, v213, vcc
	v_bitop3_b32 v16, v16, s35, v17 bitop3:0x48
	v_bitop3_b32 v16, v16, 15, v77 bitop3:0x36
	v_max_u32_e32 v17, v15, v18
	v_min_u32_e32 v15, v15, v18
	v_max_u32_e32 v18, v19, v20
	v_min_u32_e32 v19, v19, v20
	v_max_u32_e32 v20, v21, v22
	v_min_u32_e32 v21, v21, v22
	v_max_u32_e32 v22, v7, v16
	v_min_u32_e32 v7, v7, v16
	v_max_u32_e32 v16, v17, v18
	v_min_u32_e32 v17, v17, v18
	v_max_u32_e32 v18, v15, v19
	v_min_u32_e32 v15, v15, v19
	v_max_u32_e32 v19, v20, v22
	v_min_u32_e32 v20, v20, v22
	v_max_u32_e32 v22, v21, v7
	v_min_u32_e32 v7, v21, v7
	v_max_u32_e32 v21, v18, v17
	v_min_u32_e32 v17, v18, v17
	v_max_u32_e32 v18, v22, v20
	v_min_u32_e32 v20, v22, v20
	v_max_u32_e32 v22, v16, v19
	v_min_u32_e32 v16, v16, v19
	v_max_u32_e32 v19, v15, v7
	v_min_u32_e32 v7, v15, v7
	v_max_u32_e32 v15, v21, v18
	v_min_u32_e32 v18, v21, v18
	v_max_u32_e32 v21, v17, v20
	v_min_u32_e32 v17, v17, v20
	v_max_u32_e32 v20, v15, v16
	v_min_u32_e32 v15, v15, v16
	v_max_u32_e32 v16, v19, v17
	v_min_u32_e32 v17, v19, v17
	v_max_u32_e32 v19, v21, v15
	v_min_u32_e32 v15, v21, v15
	v_max_u32_e32 v21, v16, v18
	v_min_u32_e32 v16, v16, v18
	v_max_u32_e32 v18, v21, v15
	v_min_u32_e32 v15, v21, v15
	v_max_u32_dpp v21, v22, v22 quad_perm:[1,0,3,2] row_mask:0xf bank_mask:0xf bound_ctrl:1
	s_nop 1
	v_max_u32_dpp v21, v21, v21 quad_perm:[2,3,0,1] row_mask:0xf bank_mask:0xf bound_ctrl:1
	s_nop 1
	v_max_u32_dpp v21, v21, v21 row_half_mirror row_mask:0xf bank_mask:0xf bound_ctrl:1
	s_nop 1
	v_max_u32_dpp v21, v21, v21 row_mirror row_mask:0xf bank_mask:0xf bound_ctrl:1
	v_cmp_eq_u32_e32 vcc, v22, v21
	v_cndmask_b32_e64 v21, 0, v21, s[38:39]
	s_nop 0
	v_cndmask_b32_e32 v22, v22, v20, vcc
	v_cndmask_b32_e32 v20, v20, v19, vcc
	v_cndmask_b32_e32 v19, v19, v18, vcc
	v_max_u32_dpp v23, v22, v22 quad_perm:[1,0,3,2] row_mask:0xf bank_mask:0xf bound_ctrl:1
	v_cndmask_b32_e32 v18, v18, v15, vcc
	v_cndmask_b32_e32 v15, v15, v16, vcc
	v_max_u32_dpp v23, v23, v23 quad_perm:[2,3,0,1] row_mask:0xf bank_mask:0xf bound_ctrl:1
	v_cndmask_b32_e32 v16, v16, v17, vcc
	v_cndmask_b32_e32 v17, v17, v7, vcc
	v_max_u32_dpp v23, v23, v23 row_half_mirror row_mask:0xf bank_mask:0xf bound_ctrl:1
	v_cndmask_b32_e64 v7, v7, 0, vcc
	s_nop 0
	v_max_u32_dpp v23, v23, v23 row_mirror row_mask:0xf bank_mask:0xf bound_ctrl:1
	v_cmp_eq_u32_e32 vcc, v22, v23
	v_cndmask_b32_e64 v21, v21, v23, s[40:41]
	s_nop 0
	v_cndmask_b32_e32 v22, v22, v20, vcc
	v_cndmask_b32_e32 v20, v20, v19, vcc
	v_cndmask_b32_e32 v19, v19, v18, vcc
	v_max_u32_dpp v23, v22, v22 quad_perm:[1,0,3,2] row_mask:0xf bank_mask:0xf bound_ctrl:1
	v_cndmask_b32_e32 v18, v18, v15, vcc
	v_cndmask_b32_e32 v15, v15, v16, vcc
	v_max_u32_dpp v23, v23, v23 quad_perm:[2,3,0,1] row_mask:0xf bank_mask:0xf bound_ctrl:1
	v_cndmask_b32_e32 v16, v16, v17, vcc
	v_cndmask_b32_e32 v17, v17, v7, vcc
	v_max_u32_dpp v23, v23, v23 row_half_mirror row_mask:0xf bank_mask:0xf bound_ctrl:1
	v_cndmask_b32_e64 v7, v7, 0, vcc
	s_nop 0
	v_max_u32_dpp v23, v23, v23 row_mirror row_mask:0xf bank_mask:0xf bound_ctrl:1
	v_cmp_eq_u32_e32 vcc, v22, v23
	v_cndmask_b32_e64 v21, v21, v23, s[42:43]
	s_nop 0
	v_cndmask_b32_e32 v22, v22, v20, vcc
	v_cndmask_b32_e32 v20, v20, v19, vcc
	v_cndmask_b32_e32 v19, v19, v18, vcc
	v_max_u32_dpp v23, v22, v22 quad_perm:[1,0,3,2] row_mask:0xf bank_mask:0xf bound_ctrl:1
	v_cndmask_b32_e32 v18, v18, v15, vcc
	v_cndmask_b32_e32 v15, v15, v16, vcc
	v_max_u32_dpp v23, v23, v23 quad_perm:[2,3,0,1] row_mask:0xf bank_mask:0xf bound_ctrl:1
	v_cndmask_b32_e32 v16, v16, v17, vcc
	v_cndmask_b32_e32 v17, v17, v7, vcc
	v_max_u32_dpp v23, v23, v23 row_half_mirror row_mask:0xf bank_mask:0xf bound_ctrl:1
	v_cndmask_b32_e64 v7, v7, 0, vcc
	s_nop 0
	v_max_u32_dpp v23, v23, v23 row_mirror row_mask:0xf bank_mask:0xf bound_ctrl:1
	v_cmp_eq_u32_e32 vcc, v22, v23
	v_cndmask_b32_e64 v21, v21, v23, s[44:45]
	s_nop 0
	v_cndmask_b32_e32 v22, v22, v20, vcc
	v_cndmask_b32_e32 v20, v20, v19, vcc
	v_cndmask_b32_e32 v19, v19, v18, vcc
	v_max_u32_dpp v23, v22, v22 quad_perm:[1,0,3,2] row_mask:0xf bank_mask:0xf bound_ctrl:1
	v_cndmask_b32_e32 v18, v18, v15, vcc
	v_cndmask_b32_e32 v15, v15, v16, vcc
	v_max_u32_dpp v23, v23, v23 quad_perm:[2,3,0,1] row_mask:0xf bank_mask:0xf bound_ctrl:1
	v_cndmask_b32_e32 v16, v16, v17, vcc
	v_cndmask_b32_e32 v17, v17, v7, vcc
	v_max_u32_dpp v23, v23, v23 row_half_mirror row_mask:0xf bank_mask:0xf bound_ctrl:1
	v_cndmask_b32_e64 v7, v7, 0, vcc
	s_nop 0
	v_max_u32_dpp v23, v23, v23 row_mirror row_mask:0xf bank_mask:0xf bound_ctrl:1
	v_cmp_eq_u32_e32 vcc, v22, v23
	v_cndmask_b32_e64 v21, v21, v23, s[46:47]
	s_nop 0
	v_cndmask_b32_e32 v22, v22, v20, vcc
	v_cndmask_b32_e32 v20, v20, v19, vcc
	v_cndmask_b32_e32 v19, v19, v18, vcc
	v_max_u32_dpp v23, v22, v22 quad_perm:[1,0,3,2] row_mask:0xf bank_mask:0xf bound_ctrl:1
	v_cndmask_b32_e32 v18, v18, v15, vcc
	v_cndmask_b32_e32 v15, v15, v16, vcc
	v_max_u32_dpp v23, v23, v23 quad_perm:[2,3,0,1] row_mask:0xf bank_mask:0xf bound_ctrl:1
	v_cndmask_b32_e32 v16, v16, v17, vcc
	v_cndmask_b32_e32 v17, v17, v7, vcc
	v_max_u32_dpp v23, v23, v23 row_half_mirror row_mask:0xf bank_mask:0xf bound_ctrl:1
	v_cndmask_b32_e64 v7, v7, 0, vcc
	s_nop 0
	v_max_u32_dpp v23, v23, v23 row_mirror row_mask:0xf bank_mask:0xf bound_ctrl:1
	v_cmp_eq_u32_e32 vcc, v22, v23
	v_cndmask_b32_e64 v21, v21, v23, s[48:49]
	s_nop 0
	v_cndmask_b32_e32 v22, v22, v20, vcc
	v_cndmask_b32_e32 v20, v20, v19, vcc
	v_cndmask_b32_e32 v19, v19, v18, vcc
	v_max_u32_dpp v23, v22, v22 quad_perm:[1,0,3,2] row_mask:0xf bank_mask:0xf bound_ctrl:1
	v_cndmask_b32_e32 v18, v18, v15, vcc
	v_cndmask_b32_e32 v15, v15, v16, vcc
	v_max_u32_dpp v23, v23, v23 quad_perm:[2,3,0,1] row_mask:0xf bank_mask:0xf bound_ctrl:1
	v_cndmask_b32_e32 v16, v16, v17, vcc
	v_cndmask_b32_e32 v17, v17, v7, vcc
	v_max_u32_dpp v23, v23, v23 row_half_mirror row_mask:0xf bank_mask:0xf bound_ctrl:1
	v_cndmask_b32_e64 v7, v7, 0, vcc
	s_nop 0
	v_max_u32_dpp v23, v23, v23 row_mirror row_mask:0xf bank_mask:0xf bound_ctrl:1
	v_cmp_eq_u32_e32 vcc, v22, v23
	v_cndmask_b32_e64 v21, v21, v23, s[50:51]
	s_nop 0
	v_cndmask_b32_e32 v22, v22, v20, vcc
	v_cndmask_b32_e32 v20, v20, v19, vcc
	v_cndmask_b32_e32 v19, v19, v18, vcc
	v_max_u32_dpp v23, v22, v22 quad_perm:[1,0,3,2] row_mask:0xf bank_mask:0xf bound_ctrl:1
	v_cndmask_b32_e32 v18, v18, v15, vcc
	v_cndmask_b32_e32 v15, v15, v16, vcc
	v_max_u32_dpp v23, v23, v23 quad_perm:[2,3,0,1] row_mask:0xf bank_mask:0xf bound_ctrl:1
	v_cndmask_b32_e32 v16, v16, v17, vcc
	v_cndmask_b32_e32 v17, v17, v7, vcc
	v_max_u32_dpp v23, v23, v23 row_half_mirror row_mask:0xf bank_mask:0xf bound_ctrl:1
	v_cndmask_b32_e64 v7, v7, 0, vcc
	s_nop 0
	v_max_u32_dpp v23, v23, v23 row_mirror row_mask:0xf bank_mask:0xf bound_ctrl:1
	v_cmp_eq_u32_e32 vcc, v22, v23
	v_cndmask_b32_e64 v21, v21, v23, s[52:53]
	s_nop 0
	v_cndmask_b32_e32 v22, v22, v20, vcc
	v_cndmask_b32_e32 v20, v20, v19, vcc
	v_cndmask_b32_e32 v19, v19, v18, vcc
	v_max_u32_dpp v23, v22, v22 quad_perm:[1,0,3,2] row_mask:0xf bank_mask:0xf bound_ctrl:1
	v_cndmask_b32_e32 v18, v18, v15, vcc
	v_cndmask_b32_e32 v15, v15, v16, vcc
	v_max_u32_dpp v23, v23, v23 quad_perm:[2,3,0,1] row_mask:0xf bank_mask:0xf bound_ctrl:1
	v_cndmask_b32_e32 v16, v16, v17, vcc
	v_cndmask_b32_e32 v17, v17, v7, vcc
	v_max_u32_dpp v23, v23, v23 row_half_mirror row_mask:0xf bank_mask:0xf bound_ctrl:1
	v_cndmask_b32_e64 v7, v7, 0, vcc
	s_nop 0
	v_max_u32_dpp v23, v23, v23 row_mirror row_mask:0xf bank_mask:0xf bound_ctrl:1
	v_cmp_eq_u32_e32 vcc, v22, v23
	s_nop 1
	v_cndmask_b32_e32 v22, v22, v20, vcc
	v_cndmask_b32_e32 v20, v20, v19, vcc
	v_cndmask_b32_e32 v19, v19, v18, vcc
	v_cndmask_b32_e32 v18, v18, v15, vcc
	v_cndmask_b32_e32 v15, v15, v16, vcc
	v_cndmask_b32_e32 v16, v16, v17, vcc
	v_cndmask_b32_e32 v7, v17, v7, vcc
	v_cndmask_b32_e64 v17, v21, v23, s[54:55]
	v_max_u32_dpp v21, v22, v22 quad_perm:[1,0,3,2] row_mask:0xf bank_mask:0xf bound_ctrl:1
	s_nop 1
	v_max_u32_dpp v21, v21, v21 quad_perm:[2,3,0,1] row_mask:0xf bank_mask:0xf bound_ctrl:1
	s_nop 1
	v_max_u32_dpp v21, v21, v21 row_half_mirror row_mask:0xf bank_mask:0xf bound_ctrl:1
	s_nop 1
	v_max_u32_dpp v21, v21, v21 row_mirror row_mask:0xf bank_mask:0xf bound_ctrl:1
	v_cmp_eq_u32_e32 vcc, v22, v21
	s_nop 1
	v_cndmask_b32_e32 v22, v22, v20, vcc
	v_cndmask_b32_e32 v20, v20, v19, vcc
	v_cndmask_b32_e32 v19, v19, v18, vcc
	v_cndmask_b32_e32 v18, v18, v15, vcc
	v_cndmask_b32_e32 v15, v15, v16, vcc
	v_cndmask_b32_e32 v7, v16, v7, vcc
	v_cndmask_b32_e64 v16, v17, v21, s[56:57]
	v_max_u32_dpp v17, v22, v22 quad_perm:[1,0,3,2] row_mask:0xf bank_mask:0xf bound_ctrl:1
	s_nop 1
	v_max_u32_dpp v17, v17, v17 quad_perm:[2,3,0,1] row_mask:0xf bank_mask:0xf bound_ctrl:1
	s_nop 1
	v_max_u32_dpp v17, v17, v17 row_half_mirror row_mask:0xf bank_mask:0xf bound_ctrl:1
	s_nop 1
	v_max_u32_dpp v17, v17, v17 row_mirror row_mask:0xf bank_mask:0xf bound_ctrl:1
	v_cmp_eq_u32_e32 vcc, v22, v17
	s_nop 1
	v_cndmask_b32_e32 v21, v22, v20, vcc
	v_cndmask_b32_e32 v20, v20, v19, vcc
	v_cndmask_b32_e32 v19, v19, v18, vcc
	v_cndmask_b32_e32 v18, v18, v15, vcc
	v_cndmask_b32_e32 v7, v15, v7, vcc
	v_cndmask_b32_e64 v15, v16, v17, s[58:59]
	v_max_u32_dpp v16, v21, v21 quad_perm:[1,0,3,2] row_mask:0xf bank_mask:0xf bound_ctrl:1
	s_nop 1
	v_max_u32_dpp v16, v16, v16 quad_perm:[2,3,0,1] row_mask:0xf bank_mask:0xf bound_ctrl:1
	s_nop 1
	v_max_u32_dpp v16, v16, v16 row_half_mirror row_mask:0xf bank_mask:0xf bound_ctrl:1
	s_nop 1
	v_max_u32_dpp v16, v16, v16 row_mirror row_mask:0xf bank_mask:0xf bound_ctrl:1
	v_cmp_eq_u32_e32 vcc, v21, v16
	v_cndmask_b32_e64 v15, v15, v16, s[60:61]
	s_nop 0
	v_cndmask_b32_e32 v17, v21, v20, vcc
	v_cndmask_b32_e32 v20, v20, v19, vcc
	v_cndmask_b32_e32 v19, v19, v18, vcc
	v_max_u32_dpp v16, v17, v17 quad_perm:[1,0,3,2] row_mask:0xf bank_mask:0xf bound_ctrl:1
	v_cndmask_b32_e32 v7, v18, v7, vcc
	s_nop 0
	v_max_u32_dpp v16, v16, v16 quad_perm:[2,3,0,1] row_mask:0xf bank_mask:0xf bound_ctrl:1
	s_nop 1
	v_max_u32_dpp v16, v16, v16 row_half_mirror row_mask:0xf bank_mask:0xf bound_ctrl:1
	s_nop 1
	v_max_u32_dpp v16, v16, v16 row_mirror row_mask:0xf bank_mask:0xf bound_ctrl:1
	v_cmp_eq_u32_e32 vcc, v17, v16
	v_cndmask_b32_e64 v15, v15, v16, s[62:63]
	s_nop 0
	v_cndmask_b32_e32 v17, v17, v20, vcc
	v_cndmask_b32_e32 v18, v20, v19, vcc
	v_cndmask_b32_e32 v7, v19, v7, vcc
	v_max_u32_dpp v16, v17, v17 quad_perm:[1,0,3,2] row_mask:0xf bank_mask:0xf bound_ctrl:1
	s_nop 1
	v_max_u32_dpp v16, v16, v16 quad_perm:[2,3,0,1] row_mask:0xf bank_mask:0xf bound_ctrl:1
	s_nop 1
	v_max_u32_dpp v16, v16, v16 row_half_mirror row_mask:0xf bank_mask:0xf bound_ctrl:1
	s_nop 1
	v_max_u32_dpp v16, v16, v16 row_mirror row_mask:0xf bank_mask:0xf bound_ctrl:1
	v_cmp_eq_u32_e32 vcc, v17, v16
	v_cndmask_b32_e64 v15, v15, v16, s[64:65]
	s_nop 0
	v_cndmask_b32_e32 v17, v17, v18, vcc
	v_cndmask_b32_e32 v7, v18, v7, vcc
	s_nop 0
	v_max_u32_dpp v16, v17, v17 quad_perm:[1,0,3,2] row_mask:0xf bank_mask:0xf bound_ctrl:1
	s_nop 1
	v_max_u32_dpp v16, v16, v16 quad_perm:[2,3,0,1] row_mask:0xf bank_mask:0xf bound_ctrl:1
	s_nop 1
	v_max_u32_dpp v16, v16, v16 row_half_mirror row_mask:0xf bank_mask:0xf bound_ctrl:1
	s_nop 1
	v_max_u32_dpp v16, v16, v16 row_mirror row_mask:0xf bank_mask:0xf bound_ctrl:1
	v_cmp_eq_u32_e32 vcc, v17, v16
	v_cndmask_b32_e64 v15, v15, v16, s[66:67]
	s_nop 0
	v_cndmask_b32_e32 v7, v17, v7, vcc
	s_and_b64 vcc, exec, s[12:13]
	s_nop 0
	v_max_u32_dpp v7, v7, v7 quad_perm:[1,0,3,2] row_mask:0xf bank_mask:0xf bound_ctrl:1
	s_nop 1
	v_max_u32_dpp v7, v7, v7 quad_perm:[2,3,0,1] row_mask:0xf bank_mask:0xf bound_ctrl:1
	s_nop 1
	v_max_u32_dpp v7, v7, v7 row_half_mirror row_mask:0xf bank_mask:0xf bound_ctrl:1
	s_nop 1
	v_max_u32_dpp v7, v7, v7 row_mirror row_mask:0xf bank_mask:0xf bound_ctrl:1
	v_cndmask_b32_e64 v15, v15, v7, s[68:69]
	s_cbranch_vccz .LBB0_934
	ds_write_b32 v94, v15 offset:18432
	s_waitcnt lgkmcnt(0)
	v_mov_b32_e32 v7, 0
	v_mov_b32_e32 v16, 0
	s_and_saveexec_b64 s[14:15], s[70:71]
	s_cbranch_execz .LBB0_927
	ds_read_b32 v16, v96 offset:18432
	v_add_u32_e32 v17, s5, v9
	ds_read_b32 v17, v17
	s_waitcnt lgkmcnt(1)
	v_cmp_lt_i32_e32 vcc, -1, v16
	s_nop 1
	v_cndmask_b32_e64 v18, v213, -1, vcc
	s_waitcnt lgkmcnt(0)
	v_cmp_lt_i32_e32 vcc, -1, v17
	v_and_b32_e32 v17, 0xffffff80, v17
	v_and_b32_e32 v16, 0xffffff80, v16
	v_cndmask_b32_e64 v19, v213, -1, vcc
	v_xor_b32_e32 v17, v19, v17
	v_xor_b32_e32 v16, v18, v16
	v_pk_add_f32 v[16:17], v[16:17], v[16:17] op_sel:[1,0] op_sel_hi:[0,1]
	v_cmp_lt_i32_e32 vcc, -1, v16
	s_nop 1
	v_cndmask_b32_e32 v17, -1, v213, vcc
	v_bitop3_b32 v16, v17, s22, v16 bitop3:0x48
	v_sub_u32_e32 v16, v16, v90
	v_add_u32_e32 v16, 0xff, v16
